# g1b: MoE gate/up unit setup: the four gather-index loads issued together (one wait instead of four), on top of x0a
# speedup vs baseline: 1.0120x; 1.0120x over previous
; #define PG8_STAGE(bufoff, gbase, voff) do { _Pragma("unroll") for (int _i = 0; _i < 2; ++_i) \
;         __builtin_amdgcn_global_load_lds((const unsigned*)((const char*)(gbase) + (voff)[_i]), (LAS unsigned*)(lds + (bufoff) + ldsw + _i * 8192), 16, 0, 0); } while (0)
; #define PG8_STAGE_A(bufoff, gbase, h, nx) do { if constexpr (GATHER) { unsigned _v[2]; _v[0] = (nx) ? voffAn[h][0] : voffA[h][0]; _v[1] = (nx) ? voffAn[h][1] : voffA[h][1]; PG8_STAGE(bufoff, gbase, _v); } \
;         else PG8_STAGE(bufoff, (gbase) + (h) * hstepA, voffA[0]); } while (0)
; #define PG8_BAR __builtin_amdgcn_s_barrier()
; #define PG8_VOFFA(dst, u) do { if constexpr (GATHER) { _Pragma("unroll") for (int _h = 0; _h < 2; ++_h) _Pragma("unroll") for (int _i = 0; _i < 2; ++_i) { \
;         int _R, _C; stage_rc(tid * 16 + _i * 8192, _R, _C); const int _r = _h * HALF + _R; const int _t = (_r < (u).nvalid) ? (u).gidx[_r] : 0; dst[_h][_i] = (unsigned)(_t * lda + _C) * 2u; } } } while (0)
;     __device__ __forceinline__ void a_ready(const pg8::Unit& u) const { if (ready) wg_wait_counter(ready + 64 * u.pm, need, tmo, wave); }
;     __device__ __forceinline__ void a_ready(const pg8::Unit& u) const { d.a_ready(u); }
; template <class Epi, class Sched, bool GATHER, bool ALIGN_EPI>
; __device__ __forceinline__ void gemm_phase(LAS unsigned char* lds, const int wave_, const int K, const int lda, const int ldb, const Sched& S, const Epi& E) {
;     ...
;     Unit cur, nxt; int ui = 0;
;     if (!S.next(0, cur)) return;
;     PG8_VOFFA(voffA, cur);
;     f32x4 acc[2][2][4][2];
; #pragma unroll
;     for (int a = 0; a < 2; ++a)
; #pragma unroll
;         for (int b = 0; b < 2; ++b)
; #pragma unroll
;             for (int m = 0; m < 4; ++m)
; #pragma unroll
;                 for (int n = 0; n < 2; ++n) acc[a][b][m][n] = (f32x4){0.f, 0.f, 0.f, 0.f};
;     bf16x8 At[4][2], B0[2][2], B1[2][2];
;     const char* cA = cur.A; const char* cB = cur.B;
;     S.a_ready(cur);
;     PG8_STAGE(PG8_SB(0, 0), cB, voffB); PG8_STAGE(PG8_SB(0, 1), cB + hstepB, voffB); PG8_STAGE_A(PG8_SA(0, 0), cA, 0, false); PG8_STAGE_A(PG8_SA(0, 1), cA, 1, false);
;     if (wr == 1) PG8_BAR;
.LBB0_1470:
	v_readlane_b32 s2, v252, 44
	v_readlane_b32 s3, v252, 45
	s_mul_i32 s64, s2, 0x2800
	s_lshl_b64 s[2:3], s[64:65], 2
	v_readlane_b32 s8, v253, 26
	s_add_u32 s30, s8, s2
	v_readlane_b32 s2, v253, 27
	s_addc_u32 s31, s2, s3
	s_andn2_b64 vcc, exec, s[0:1]
	s_cbranch_vccnz .LBB0_1523
	v_ashrrev_i32_e32 v0, 31, v8
	v_lshrrev_b32_e32 v0, 26, v0
	v_add_u32_e32 v0, v8, v0
	v_ashrrev_i32_e32 v1, 6, v0
	v_bfe_i32 v0, v8, 27, 1
	v_lshlrev_b32_e32 v5, 4, v8
	v_lshrrev_b32_e32 v0, 22, v0
	v_add_u32_e32 v0, v5, v0
	v_and_b32_e32 v0, 0xfffffc00, v0
	v_sub_u32_e32 v0, v5, v0
	v_lshrrev_b32_e32 v2, 4, v0
	v_bitop3_b32 v2, v2, v0, 32 bitop3:0x6c
	v_lshlrev_b32_e32 v0, 3, v1
	v_and_b32_e32 v3, -16, v0
	v_ashrrev_i32_e32 v0, 31, v2
	v_lshrrev_b32_e32 v0, 26, v0
	v_add_u32_e32 v0, v2, v0
	v_ashrrev_i32_e32 v0, 6, v0
	v_add_u32_e32 v152, v0, v3
	v_cmp_gt_i32_e32 vcc, s36, v152
	v_mov_b32_e32 v3, 0
	v_ashrrev_i32_e32 v153, 31, v152
	v_mov_b32_e32 v4, 0
	s_and_saveexec_b64 s[0:1], vcc
	s_cbranch_execz .LBB0_1473
	v_lshl_add_u64 v[6:7], v[152:153], 2, s[6:7]
	global_load_dword v4, v[6:7], off
.LBB0_1473:
	s_or_b64 exec, exec, s[0:1]
	v_add_u32_e32 v5, 0x2000, v5
	v_ashrrev_i32_e32 v6, 31, v5
	v_lshrrev_b32_e32 v6, 22, v6
	v_add_u32_e32 v6, v5, v6
	v_ashrrev_i32_e32 v6, 10, v6
	v_mul_i32_i24_e32 v7, 0x400, v6
	v_sub_u32_e32 v5, v5, v7
	v_lshrrev_b32_e32 v7, 4, v5
	v_bitop3_b32 v7, v7, v5, 32 bitop3:0x6c
	v_lshlrev_b32_e32 v5, 3, v6
	v_and_b32_e32 v9, -16, v5
	v_ashrrev_i32_e32 v5, 31, v7
	v_lshrrev_b32_e32 v5, 26, v5
	v_add_u32_e32 v5, v7, v5
	v_ashrrev_i32_e32 v5, 6, v5
	v_add_u32_e32 v154, v5, v9
	v_cmp_gt_i32_e32 vcc, s36, v154
	v_ashrrev_i32_e32 v155, 31, v154
	s_and_saveexec_b64 s[0:1], vcc
	s_cbranch_execz .LBB0_1475
	v_lshl_add_u64 v[10:11], v[154:155], 2, s[6:7]
	global_load_dword v3, v[10:11], off
.LBB0_1475:
	s_or_b64 exec, exec, s[0:1]
	v_add_u32_e32 v163, 0x80, v152
	v_cmp_gt_i32_e32 vcc, s36, v163
	v_mov_b32_e32 v9, 0
	v_mov_b32_e32 v10, 0
	s_and_saveexec_b64 s[0:1], vcc
	s_cbranch_execz .LBB0_1477
	v_lshl_add_u64 v[10:11], v[152:153], 2, s[6:7]
	global_load_dword v10, v[10:11], off offset:512
.LBB0_1477:
	s_or_b64 exec, exec, s[0:1]
	v_add_u32_e32 v180, 0x80, v154
	v_cmp_gt_i32_e32 vcc, s36, v180
	s_and_saveexec_b64 s[0:1], vcc
	s_cbranch_execz .LBB0_1479
	v_lshl_add_u64 v[12:13], v[154:155], 2, s[6:7]
	global_load_dword v9, v[12:13], off offset:512
.LBB0_1479:
	s_or_b64 exec, exec, s[0:1]
	s_waitcnt vmcnt(0)
	v_lshlrev_b32_e32 v4, 10, v4
	v_lshlrev_b32_e32 v3, 10, v3
	v_lshlrev_b32_e32 v10, 10, v10
	v_lshlrev_b32_e32 v9, 10, v9
	v_lshlrev_b32_e32 v11, 6, v0
	v_lshlrev_b32_e32 v1, 5, v1
	v_sub_u32_e32 v2, v2, v11
	v_and_b32_e32 v1, 32, v1
	v_ashrrev_i16_sdwa v2, v249, sext(v2) dst_sel:DWORD dst_unused:UNUSED_PAD src0_sel:DWORD src1_sel:BYTE_0
	v_add_u32_sdwa v181, v1, sext(v2) dst_sel:DWORD dst_unused:UNUSED_PAD src0_sel:DWORD src1_sel:WORD_0
	v_lshlrev_b32_e32 v2, 6, v5
	v_lshlrev_b32_e32 v1, 5, v6
	v_sub_u32_e32 v2, v7, v2
	v_and_b32_e32 v1, 32, v1
	v_ashrrev_i16_sdwa v2, v249, sext(v2) dst_sel:DWORD dst_unused:UNUSED_PAD src0_sel:DWORD src1_sel:BYTE_0
	v_add_u32_sdwa v182, v1, sext(v2) dst_sel:DWORD dst_unused:UNUSED_PAD src0_sel:DWORD src1_sel:WORD_0
	v_lshlrev_b32_e32 v1, 1, v152
	v_lshrrev_b32_e32 v2, 2, v152
	v_and_b32_e32 v0, 3, v0
	s_mov_b32 s0, 0x1fffe0
	v_and_b32_e32 v1, 24, v1
	v_and_b32_e32 v2, 4, v2
	v_and_or_b32 v0, v152, s0, v0
	v_or3_b32 v0, v0, v2, v1
	v_lshlrev_b32_e32 v1, 1, v181
	v_lshl_add_u32 v156, v0, 11, v1
	v_lshlrev_b32_e32 v0, 1, v154
	v_lshrrev_b32_e32 v1, 2, v154
	v_and_b32_e32 v2, 3, v5
	s_add_i32 s37, s62, 0
	v_and_b32_e32 v0, 24, v0
	v_and_b32_e32 v1, 4, v1
	v_and_or_b32 v2, v154, s0, v2
	s_add_i32 m0, s37, 0x10000
	v_or3_b32 v0, v2, v1, v0
	v_lshlrev_b32_e32 v1, 1, v182
	global_load_lds_dwordx4 v156, s[4:5]
	s_add_i32 m0, s37, 0x12000
	v_lshl_add_u32 v158, v0, 11, v1
	s_add_u32 s0, s4, 0x40000
	global_load_lds_dwordx4 v158, s[4:5]
	s_addc_u32 s1, s5, 0
	s_add_i32 m0, s37, 0x14000
	v_add_lshl_u32 v170, v4, v181, 1
	global_load_lds_dwordx4 v156, s[0:1]
	s_add_i32 m0, s37, 0x16000
	s_add_i32 s38, s37, 0x2000
	global_load_lds_dwordx4 v158, s[0:1]
	s_mov_b32 m0, s37
	v_add_lshl_u32 v168, v3, v182, 1
	global_load_lds_dwordx4 v170, s[12:13]
	s_mov_b32 m0, s38
	s_add_i32 s39, s37, 0x4000
	v_add_lshl_u32 v164, v10, v181, 1
	global_load_lds_dwordx4 v168, s[12:13]
	s_mov_b32 m0, s39
	s_add_i32 s40, s37, 0x6000
	v_add_lshl_u32 v172, v9, v182, 1
	global_load_lds_dwordx4 v164, s[12:13]
	s_mov_b32 m0, s40
	v_readlane_b32 s0, v252, 46
	global_load_lds_dwordx4 v172, s[12:13]
	v_mov_b32_e32 v157, v161
	v_mov_b32_e32 v159, v161
	v_mov_b32_e32 v171, v161
	v_mov_b32_e32 v169, v161
	v_readlane_b32 s1, v252, 47
	v_lshl_add_u64 v[6:7], s[4:5], 0, v[156:157]
	v_lshl_add_u64 v[4:5], s[4:5], 0, v[158:159]
	v_lshl_add_u64 v[0:1], s[12:13], 0, v[170:171]
	s_and_b64 vcc, exec, s[0:1]
	v_lshl_add_u64 v[2:3], s[12:13], 0, v[168:169]
	s_cbranch_vccnz .LBB0_1481
	s_barrier
